# one static s_setprio 1 for waves 4-7 in the non-GEMM MFMA phases (attention, token+lora, scan R1, R3), reset at the following barrier
# speedup vs baseline: 1.0129x; 1.0129x over previous
.LBB0_607:
	s_or_b64 exec, exec, s[0:1]
	s_waitcnt lgkmcnt(0)
	s_barrier
	v_cmp_lt_u32_e32 vcc, 0xff, v0
	s_cbranch_vccz .Lprio_1
	s_setprio 1
.Lprio_1:
.LBB0_608:
	s_cmp_gt_i32 s50, 2
	s_cselect_b64 s[0:1], -1, 0
	s_cmp_lt_i32 s51, 3
	s_cselect_b64 s[2:3], -1, 0
	s_or_b64 s[2:3], s[0:1], s[2:3]
	s_and_b64 vcc, exec, s[2:3]
	v_readlane_b32 s76, v253, 0
	v_readlane_b32 s77, v253, 1
	s_cbranch_vccnz .LBB0_648
	v_writelane_b32 v252, s2, 15
	s_cmpk_lt_i32 s76, 0x200
	s_cselect_b64 s[0:1], -1, 0
	v_writelane_b32 v252, s3, 16
	v_writelane_b32 v252, s90, 17
	v_writelane_b32 v252, s0, 18
	s_cmpk_gt_i32 s76, 0x1ff
	s_nop 0
	v_writelane_b32 v252, s1, 19
	s_cbranch_scc1 .LBB0_626
	s_add_u32 s28, s48, 0xa800000
	s_addc_u32 s29, s49, 0
	s_add_u32 s94, s48, 0xb800000
	s_addc_u32 s95, s49, 0
	s_add_u32 s76, s48, 0x10000000
	s_addc_u32 s85, s49, 0
	s_add_u32 s35, s48, 0x6800400
	v_readlane_b32 s6, v253, 0
	s_addc_u32 s36, s49, 0
	s_lshl_b32 s0, s6, 8
	s_and_b32 s4, s0, 0x2000
	s_and_b32 s0, s0, 0x1f00
	s_add_i32 s5, s0, 0xffffff80
	s_ashr_i32 s0, s6, 8
	s_ashr_i32 s1, s0, 31
	v_mov_b32_e32 v10, v0
	s_lshl_b64 s[2:3], s[0:1], 21
	s_add_u32 s0, s76, s2
	v_ashrrev_i32_e32 v1, 3, v10
	v_add_u32_e32 v2, s5, v1
	v_mov_b32_e32 v1, 0x1fff
	s_addc_u32 s1, s85, s3
	v_med3_i32 v2, v2, 0, v1
	s_add_u32 s2, s94, s2
	v_or_b32_e32 v2, s4, v2
	s_addc_u32 s3, s95, s3
	v_lshlrev_b32_e32 v2, 7, v2
	v_mov_b32_e32 v3, 0
	v_lshl_add_u64 v[4:5], s[2:3], 0, v[2:3]
	v_lshl_add_u64 v[8:9], s[0:1], 0, v[2:3]
	v_add_u32_e32 v2, 0x200, v10
	v_ashrrev_i32_e32 v2, 3, v2
	v_add_u32_e32 v2, s5, v2
	v_lshlrev_b32_e32 v6, 4, v10
	v_med3_i32 v2, v2, 0, v1
	v_and_b32_e32 v6, 0x70, v6
	v_mov_b32_e32 v7, v3
	v_or_b32_e32 v2, s4, v2
	v_lshl_add_u64 v[4:5], v[4:5], 0, v[6:7]
	v_lshl_add_u64 v[8:9], v[8:9], 0, v[6:7]
	v_lshlrev_b32_e32 v2, 7, v2
	global_load_dwordx4 v[56:59], v[4:5], off
	global_load_dwordx4 v[52:55], v[8:9], off
	v_lshl_add_u64 v[4:5], s[2:3], 0, v[2:3]
	v_lshl_add_u64 v[8:9], s[0:1], 0, v[2:3]
	v_add_u32_e32 v2, 0x400, v10
	v_ashrrev_i32_e32 v2, 3, v2
	v_add_u32_e32 v2, s5, v2
	v_med3_i32 v2, v2, 0, v1
	v_or_b32_e32 v2, s4, v2
	v_lshl_add_u64 v[4:5], v[4:5], 0, v[6:7]
	v_lshl_add_u64 v[8:9], v[8:9], 0, v[6:7]
	v_lshlrev_b32_e32 v2, 7, v2
	global_load_dwordx4 v[64:67], v[4:5], off
	global_load_dwordx4 v[60:63], v[8:9], off
	v_lshl_add_u64 v[4:5], s[2:3], 0, v[2:3]
	v_lshl_add_u64 v[8:9], s[0:1], 0, v[2:3]
	v_add_u32_e32 v2, 0x600, v10
	v_ashrrev_i32_e32 v2, 3, v2
	v_add_u32_e32 v2, s5, v2
	v_med3_i32 v2, v2, 0, v1
	v_or_b32_e32 v2, s4, v2
	v_lshl_add_u64 v[4:5], v[4:5], 0, v[6:7]
	v_lshl_add_u64 v[8:9], v[8:9], 0, v[6:7]
	v_lshlrev_b32_e32 v2, 7, v2
	global_load_dwordx4 v[72:75], v[4:5], off
	global_load_dwordx4 v[68:71], v[8:9], off
	v_lshl_add_u64 v[4:5], s[2:3], 0, v[2:3]
	v_lshl_add_u64 v[8:9], s[0:1], 0, v[2:3]
	v_add_u32_e32 v2, 0x800, v10
	v_ashrrev_i32_e32 v2, 3, v2
	v_add_u32_e32 v2, s5, v2
	v_med3_i32 v2, v2, 0, v1
	v_or_b32_e32 v2, s4, v2
	v_lshl_add_u64 v[4:5], v[4:5], 0, v[6:7]
	v_lshl_add_u64 v[8:9], v[8:9], 0, v[6:7]
	v_lshlrev_b32_e32 v2, 7, v2
	global_load_dwordx4 v[80:83], v[4:5], off
	global_load_dwordx4 v[76:79], v[8:9], off
	v_lshl_add_u64 v[4:5], s[2:3], 0, v[2:3]
	v_lshl_add_u64 v[8:9], s[0:1], 0, v[2:3]
	v_add_u32_e32 v2, 0xa00, v10
	v_ashrrev_i32_e32 v2, 3, v2
	v_add_u32_e32 v2, s5, v2
	v_med3_i32 v2, v2, 0, v1
	v_or_b32_e32 v2, s4, v2
	v_lshl_add_u64 v[4:5], v[4:5], 0, v[6:7]
	v_lshl_add_u64 v[8:9], v[8:9], 0, v[6:7]
	v_lshlrev_b32_e32 v2, 7, v2
	global_load_dwordx4 v[88:91], v[4:5], off
	global_load_dwordx4 v[84:87], v[8:9], off
	v_lshl_add_u64 v[4:5], s[2:3], 0, v[2:3]
	v_lshl_add_u64 v[8:9], s[0:1], 0, v[2:3]
	v_add_u32_e32 v2, 0xc00, v10
	v_ashrrev_i32_e32 v2, 3, v2
	v_add_u32_e32 v2, s5, v2
	v_med3_i32 v2, v2, 0, v1
	v_or_b32_e32 v2, s4, v2
	v_lshl_add_u64 v[4:5], v[4:5], 0, v[6:7]
	v_lshl_add_u64 v[8:9], v[8:9], 0, v[6:7]
	v_lshlrev_b32_e32 v2, 7, v2
	global_load_dwordx4 v[96:99], v[4:5], off
	global_load_dwordx4 v[92:95], v[8:9], off
	v_lshl_add_u64 v[4:5], s[2:3], 0, v[2:3]
	v_lshl_add_u64 v[8:9], s[0:1], 0, v[2:3]
	v_add_u32_e32 v2, 0xe00, v10
	v_ashrrev_i32_e32 v2, 3, v2
	v_add_u32_e32 v2, s5, v2
	v_med3_i32 v2, v2, 0, v1
	v_or_b32_e32 v2, s4, v2
	v_lshl_add_u64 v[4:5], v[4:5], 0, v[6:7]
	v_lshlrev_b32_e32 v2, 7, v2
	v_lshl_add_u64 v[8:9], v[8:9], 0, v[6:7]
	global_load_dwordx4 v[104:107], v[4:5], off
	global_load_dwordx4 v[100:103], v[8:9], off
	v_lshl_add_u64 v[4:5], s[2:3], 0, v[2:3]
	v_lshl_add_u64 v[4:5], v[4:5], 0, v[6:7]
	v_lshl_add_u64 v[8:9], s[0:1], 0, v[2:3]
	v_lshl_add_u64 v[6:7], v[8:9], 0, v[6:7]
	global_load_dwordx4 v[112:115], v[4:5], off
	global_load_dwordx4 v[108:111], v[6:7], off
	v_writelane_b32 v252, s35, 20
	s_mov_b32 s93, 0
	s_add_i32 s37, 0, 0x12000
	s_movk_i32 s96, 0x90
	s_movk_i32 s97, 0x88
	v_mov_b32_e32 v134, 0xf149f2ca
	s_mov_b32 s77, s6
	v_writelane_b32 v252, s36, 22
	v_readlane_b32 s7, v253, 1
	v_writelane_b32 v252, s37, 24
	s_branch .LBB0_612

.LBB0_697:
	s_or_b64 exec, exec, s[0:1]
	s_waitcnt lgkmcnt(0)
	s_barrier
	s_setprio 0

.Lprio_12:
.LBB0_1674:
	s_add_u32 s60, s48, 0x18800000
	s_addc_u32 s61, s49, 0
	s_add_u32 s92, s48, 0x1c800000
	s_addc_u32 s93, s49, 0
	s_add_u32 s58, s48, 0x24800000
	s_addc_u32 s59, s49, 0
	s_add_u32 s68, s48, 0x26800000
	s_addc_u32 s69, s49, 0
	s_add_u32 s2, s48, 0x2c800000
	s_addc_u32 s3, s49, 0
	s_add_u32 s52, s48, 0x30800000
	s_addc_u32 s53, s49, 0
	s_cmp_gt_i32 s50, 12
	s_cselect_b64 s[0:1], -1, 0
	s_cmp_lt_i32 s51, 13
	s_cselect_b64 s[4:5], -1, 0
	s_or_b64 s[36:37], s[0:1], s[4:5]
	s_and_b64 vcc, exec, s[36:37]
	s_cbranch_vccnz .LBB0_1773
	s_waitcnt lgkmcnt(0)
	v_mov_b32_e32 v3, v0
	s_add_u32 s34, s48, 0x31800000
	v_ashrrev_i32_e32 v2, 3, v3
	v_and_b32_e32 v2, -8, v2
	v_lshl_add_u32 v2, s76, 6, v2
	s_movk_i32 s0, 0x4000
	s_addc_u32 s35, s49, 0
	v_cmp_gt_i32_e32 vcc, s0, v2
	s_and_saveexec_b64 s[30:31], vcc
	s_cbranch_execz .LBB0_1710
	v_lshlrev_b32_e32 v3, 1, v3
	s_lshl_b32 s20, s91, 6
	v_and_b32_e32 v4, 0x7e, v3
	s_mov_b64 s[16:17], s[2:3]
	v_readlane_b32 s0, v253, 45
	s_waitcnt vmcnt(0)
	v_or_b32_e32 v114, 0x700, v4
	v_readlane_b32 s1, v253, 46
	s_add_u32 s0, s80, 0x1e00
	v_lshlrev_b32_e32 v3, 2, v4
	v_or_b32_e32 v110, 0x600, v4
	v_or_b32_e32 v112, 0x680, v4
	v_readlane_b32 s4, v253, 49
	v_readlane_b32 s5, v253, 50
	s_addc_u32 s1, s81, 0
	v_lshlrev_b32_e32 v5, 2, v114
	v_or_b32_e32 v106, 0x500, v4
	v_or_b32_e32 v108, 0x580, v4
	s_nop 0
	global_load_dwordx2 v[6:7], v3, s[4:5] offset:1536
	global_load_dwordx2 v[8:9], v3, s[4:5] offset:1024
	global_load_dwordx2 v[10:11], v3, s[4:5] offset:512
	global_load_dwordx2 v[12:13], v3, s[4:5]
	v_lshlrev_b32_e32 v18, 2, v112
	global_load_dwordx2 v[14:15], v5, s[0:1]
	global_load_dwordx2 v[16:17], v18, s[80:81]
	global_load_dwordx2 v[92:93], v5, s[80:81]
	v_lshlrev_b32_e32 v5, 2, v110
	v_or_b32_e32 v102, 0x400, v4
	v_or_b32_e32 v104, 0x480, v4
	v_lshlrev_b32_e32 v24, 2, v108
	global_load_dwordx2 v[18:19], v18, s[0:1]
	s_nop 0
	global_load_dwordx2 v[20:21], v5, s[0:1]
	global_load_dwordx2 v[22:23], v24, s[80:81]
	global_load_dwordx2 v[90:91], v5, s[80:81]
	v_lshlrev_b32_e32 v5, 2, v106
	v_lshlrev_b32_e32 v32, 2, v104
	global_load_dwordx2 v[24:25], v24, s[0:1]
	s_nop 0
	global_load_dwordx2 v[26:27], v5, s[0:1]
	global_load_dwordx2 v[28:29], v32, s[80:81]
	global_load_dwordx2 v[30:31], v5, s[80:81]
	v_lshlrev_b32_e32 v5, 2, v102
	v_or_b32_e32 v36, 0xe00, v3
	global_load_dwordx2 v[32:33], v32, s[0:1]
	s_nop 0
	global_load_dwordx2 v[34:35], v5, s[0:1]
	s_nop 0
	global_load_dwordx2 v[36:37], v36, s[0:1]
	s_nop 0
	global_load_dwordx2 v[38:39], v5, s[80:81]
	v_or_b32_e32 v5, 0xc00, v3
	v_or_b32_e32 v50, 0xa00, v3
	v_or_b32_e32 v52, 0x800, v3
	v_or_b32_e32 v54, 0x600, v3
	global_load_dwordx2 v[40:41], v3, s[80:81] offset:3584
	global_load_dwordx2 v[42:43], v3, s[80:81] offset:3072
	global_load_dwordx2 v[44:45], v3, s[80:81] offset:2560
	global_load_dwordx2 v[46:47], v3, s[80:81] offset:2048
	global_load_dwordx2 v[48:49], v5, s[0:1]
	s_nop 0
	global_load_dwordx2 v[50:51], v50, s[0:1]
	s_nop 0
	global_load_dwordx2 v[52:53], v52, s[0:1]
	s_nop 0
	global_load_dwordx2 v[54:55], v54, s[0:1]
	v_or_b32_e32 v5, 0x400, v3
	v_or_b32_e32 v66, 0x200, v3
	global_load_dwordx2 v[56:57], v3, s[72:73] offset:1536
	global_load_dwordx2 v[58:59], v3, s[74:75] offset:1536
	global_load_dwordx2 v[60:61], v3, s[80:81] offset:1536
	global_load_dwordx2 v[62:63], v3, s[80:81] offset:1024
	global_load_dwordx2 v[64:65], v5, s[0:1]
	s_nop 0
	global_load_dwordx2 v[66:67], v66, s[0:1]
	s_nop 0
	global_load_dwordx2 v[68:69], v3, s[74:75] offset:512
	global_load_dwordx2 v[70:71], v3, s[72:73] offset:1024
	global_load_dwordx2 v[72:73], v3, s[74:75] offset:1024
	global_load_dwordx2 v[74:75], v3, s[80:81] offset:512
	global_load_dwordx2 v[76:77], v3, s[0:1]
	global_load_dwordx2 v[78:79], v3, s[72:73]
	global_load_dwordx2 v[80:81], v3, s[74:75]
	global_load_dwordx2 v[82:83], v3, s[72:73] offset:512
	global_load_dwordx2 v[84:85], v3, s[80:81]
	v_mbcnt_lo_u32_b32 v3, -1, 0
	v_mbcnt_hi_u32_b32 v3, -1, v3
	v_and_b32_e32 v5, 64, v3
	v_add_u32_e32 v86, 64, v5
	v_xor_b32_e32 v5, 32, v3
	v_cmp_lt_i32_e32 vcc, v5, v86
	v_xor_b32_e32 v88, 16, v3
	v_readlane_b32 s2, v253, 47
	v_cndmask_b32_e32 v5, v3, v5, vcc
	v_cmp_lt_i32_e32 vcc, v88, v86
	v_readlane_b32 s3, v253, 48
	v_mov_b32_e32 v87, 0
	v_cndmask_b32_e32 v88, v3, v88, vcc
	v_lshlrev_b32_e32 v142, 2, v88
	v_xor_b32_e32 v88, 8, v3
	v_cmp_lt_i32_e32 vcc, v88, v86
	s_mov_b64 s[2:3], s[16:17]
	s_mov_b64 s[0:1], 0x16800000
	v_cndmask_b32_e32 v88, v3, v88, vcc
	v_lshlrev_b32_e32 v143, 2, v88
	v_xor_b32_e32 v88, 4, v3
	v_cmp_lt_i32_e32 vcc, v88, v86
	v_lshlrev_b32_e32 v5, 2, v5
	s_mov_b64 s[16:17], 0
	v_cndmask_b32_e32 v88, v3, v88, vcc
	v_lshlrev_b32_e32 v144, 2, v88
	v_xor_b32_e32 v88, 2, v3
	v_cmp_lt_i32_e32 vcc, v88, v86
	s_movk_i32 s21, 0x1800
	s_mov_b64 s[18:19], 0x800
	v_cndmask_b32_e32 v88, v3, v88, vcc
	v_lshlrev_b32_e32 v145, 2, v88
	v_xor_b32_e32 v88, 1, v3
	v_cmp_lt_i32_e32 vcc, v88, v86
	v_lshlrev_b32_e32 v86, 1, v4
	v_lshl_add_u64 v[96:97], s[48:49], 0, v[86:87]
	v_cndmask_b32_e32 v3, v3, v88, vcc
	v_lshlrev_b32_e32 v146, 2, v3
	v_lshl_add_u64 v[94:95], s[2:3], 0, v[86:87]
	v_lshl_add_u64 v[96:97], v[96:97], 0, s[0:1]
	v_lshl_add_u64 v[98:99], s[58:59], 0, v[86:87]
	v_lshl_add_u64 v[100:101], s[34:35], 0, v[86:87]
	s_movk_i32 s22, 0x3fff
	v_mov_b32_e32 v147, 0x3727c5ac
	s_mov_b32 s23, 0x800000
	s_mov_b32 s24, 0xf800000
	v_mov_b32_e32 v148, 0x260
	s_movk_i32 s25, 0x300
	s_movk_i32 s26, 0x1fff
	v_lshlrev_b32_e32 v102, 1, v102
	v_lshlrev_b32_e32 v104, 1, v104
	v_lshlrev_b32_e32 v106, 1, v106
	v_lshlrev_b32_e32 v108, 1, v108
	v_lshlrev_b32_e32 v110, 1, v110
	v_lshlrev_b32_e32 v112, 1, v112
	v_lshlrev_b32_e32 v114, 1, v114
	v_mov_b32_e32 v149, 0x1800
	v_readlane_b32 s6, v253, 51
	v_readlane_b32 s7, v253, 52
	v_readlane_b32 s8, v253, 53
	v_readlane_b32 s9, v253, 54
	s_waitcnt vmcnt(33)
	v_mov_b32_e32 v89, v20
	v_readlane_b32 s10, v253, 55
	s_waitcnt vmcnt(31)
	v_mov_b32_e32 v88, v90
	v_mov_b32_e32 v20, v91
	v_mov_b32_e32 v90, v92
	v_mov_b32_e32 v91, v14
	v_mov_b32_e32 v14, v93
	v_lshl_add_u64 v[92:93], s[52:53], 0, v[86:87]
	v_readlane_b32 s11, v253, 56
	v_readlane_b32 s12, v253, 57
	v_readlane_b32 s13, v253, 58
	v_readlane_b32 s14, v253, 59
	v_readlane_b32 s15, v253, 60

.Lprio_13:
.LBB0_1823:
	s_cmp_gt_i32 s50, 13
	s_cselect_b64 s[0:1], -1, 0
	s_cmp_lt_i32 s51, 14
	s_cselect_b64 s[4:5], -1, 0
	s_or_b64 s[72:73], s[0:1], s[4:5]
	s_and_b64 vcc, exec, s[72:73]
	s_cbranch_vccnz .LBB0_1859
	s_cmpk_gt_i32 s76, 0x1ff
	v_mov_b32_e32 v2, v0
	s_cbranch_scc1 .LBB0_1827
	v_bfe_u32 v6, v2, 4, 2
	s_waitcnt vmcnt(0)
	v_ashrrev_i32_e32 v118, 2, v2
	s_waitcnt lgkmcnt(0)
	v_lshlrev_b32_e32 v3, 5, v2
	v_mov_b32_e32 v75, 0
	v_lshlrev_b32_e32 v74, 4, v6
	v_and_b32_e32 v5, 15, v2
	v_and_b32_e32 v4, 0x60, v3
	v_bfi_b32 v76, -16, v118, v2
	v_lshl_add_u64 v[2:3], s[48:49], 0, v[74:75]
	s_mov_b64 s[0:1], 0x32400000
	v_lshl_add_u64 v[78:79], v[2:3], 0, s[0:1]
	s_movk_i32 s0, 0x110
	v_lshlrev_b32_e32 v7, 1, v118
	v_add_u32_e32 v2, 0, v74
	v_mad_u32_u24 v3, v4, s0, 0
	v_mul_u32_u24_e32 v5, 0x110, v5
	v_ashrrev_i32_e32 v77, 31, v76
	s_mov_b32 s1, 0
	v_lshlrev_b32_e32 v119, 2, v6
	s_lshl_b32 s6, s76, 7
	s_lshl_b32 s7, s91, 7
	v_lshlrev_b32_e32 v80, 1, v4
	v_mov_b32_e32 v81, v75
	v_add_u32_e32 v120, v3, v7
	s_movk_i32 s10, 0x1800
	v_mov_b64_e32 v[82:83], s[80:81]
	v_add_u32_e32 v121, v2, v5
	s_mov_b32 s11, s76

.Lprio_15:
.LBB0_1977:
	s_cmp_gt_i32 s50, 15
	s_cselect_b64 s[0:1], -1, 0
	s_cmp_lt_i32 s51, 16
	s_cselect_b64 s[4:5], -1, 0
	s_or_b64 s[0:1], s[0:1], s[4:5]
	s_and_b64 vcc, exec, s[0:1]
	s_cbranch_vccnz .LBB0_1984
	s_waitcnt vmcnt(0)
	v_mov_b32_e32 v2, v0
	v_readlane_b32 s4, v253, 0
	v_ashrrev_i32_e32 v1, 8, v2
	v_readlane_b32 s5, v253, 1
	v_lshl_add_u32 v1, s4, 1, v1
	s_movk_i32 s4, 0x800
	v_cmp_gt_i32_e32 vcc, s4, v1
	s_and_saveexec_b64 s[4:5], vcc
	s_cbranch_execz .LBB0_1983
	s_waitcnt lgkmcnt(0)
	v_and_b32_e32 v3, 15, v2
	v_bfe_u32 v5, v2, 4, 2
	v_lshrrev_b32_e32 v2, 2, v2
	v_and_or_b32 v22, v2, 48, v3
	v_mbcnt_lo_u32_b32 v2, -1, 0
	v_mbcnt_hi_u32_b32 v2, -1, v2
	v_and_b32_e32 v8, 64, v2
	v_lshlrev_b32_e32 v4, 3, v5
	v_lshlrev_b32_e32 v18, 4, v5
	v_lshlrev_b32_e32 v20, 2, v5
	v_xor_b32_e32 v5, 16, v2
	v_add_u32_e32 v8, 64, v8
	v_cmp_lt_i32_e32 vcc, v5, v8
	s_add_u32 s6, s48, 0x12800000
	v_mov_b32_e32 v19, 0
	v_cndmask_b32_e32 v5, v2, v5, vcc
	v_lshlrev_b32_e32 v21, 2, v5
	v_xor_b32_e32 v5, 32, v2
	v_cmp_lt_i32_e32 vcc, v5, v8
	s_addc_u32 s7, s49, 0
	v_lshl_add_u64 v[6:7], s[48:49], 0, v[18:19]
	v_cndmask_b32_e32 v2, v2, v5, vcc
	v_lshlrev_b32_e32 v18, 7, v3
	s_add_u32 s8, s48, 0x16800000
	v_lshlrev_b32_e32 v23, 2, v2
	v_lshlrev_b32_e32 v46, 6, v22
	v_lshl_add_u64 v[2:3], v[6:7], 0, v[18:19]
	s_mov_b64 s[10:11], 0x14800000
	s_addc_u32 s9, s49, 0
	s_lshl_b32 s16, s91, 1
	v_xor_b32_e32 v47, 0xfc0, v46
	v_lshl_add_u64 v[24:25], v[2:3], 0, s[10:11]
	s_mov_b64 s[10:11], 0
	v_lshlrev_b32_e32 v26, 1, v4
	v_mov_b32_e32 v27, v19
	v_lshlrev_b32_e32 v28, 1, v20
	v_mov_b32_e32 v29, v19
	s_movk_i32 s17, 0x1000
	s_mov_b64 s[12:13], 0x1000000
	v_mov_b32_e32 v48, 0x3a27c5ac
	s_mov_b32 s18, 0x800000
	s_movk_i32 s19, 0x7ff
